# v88 with the barrier's L1 invalidate issued right behind the arrival atomic (all waves parked, nothing refills L1 before release): overlaps the ~1 us invalidate with the wait
# speedup vs baseline: 1.0021x; 1.0021x over previous
; __device__ __forceinline__ unsigned xb_ld(unsigned* p)              { return __hip_atomic_load(p, __ATOMIC_RELAXED, __HIP_MEMORY_SCOPE_AGENT); }
; __device__ __forceinline__ unsigned xb_add(unsigned* p, unsigned v) { return __hip_atomic_fetch_add(p, v, __ATOMIC_RELAXED, __HIP_MEMORY_SCOPE_AGENT); }
; #define XB_SPIN(cond, bar) do { unsigned _sp = 0; while (cond) { __builtin_amdgcn_s_sleep(1); \
;     if ((++_sp & 255u) == 0u) { if (xb_ld(&(bar)[XB_TMO])) break; if (_sp > XB_SPIN_CAP) { atomicAdd(&(bar)[XB_TMO], 1u); break; } } } } while (0)
; #define XB_TID() ((int)__builtin_amdgcn_mbcnt_hi(~0u, __builtin_amdgcn_mbcnt_lo(~0u, 0u)) + 64 * xb_wave_id)
; __device__ __forceinline__ void xcd_barrier(const XcdBarrier& b, const int xb_wave_id) {
;     asm volatile("s_waitcnt vmcnt(0)" ::: "memory");
;     __syncthreads();
;     if (XB_TID() == 0) {
;         unsigned* bar = b.bar;
;         __builtin_amdgcn_s_waitcnt(0);
;         unsigned nloc = b.st[0], nx = b.st[1];
;         if (nloc == 0u) { xcd_barrier_complete(bar, b.x, nloc, nx); b.st[0] = nloc; b.st[1] = nx; }
;         const unsigned old = xb_add(&bar[XB_XSUB(b.x)], 1u);
;         const unsigned gen = old / nloc;
;         if (old + 1u == (gen + 1u) * nloc) {
;             __builtin_amdgcn_fence(__ATOMIC_RELEASE, "agent");
;             asm volatile("s_waitcnt vmcnt(0)" ::: "memory");
;             const unsigned og = xb_add(&bar[XB_TOP], 1u);
;             const unsigned tg = og / nx;
;             if (og + 1u == (tg + 1u) * nx) xb_add(&bar[XB_TOPGEN], 1u);
;             else XB_SPIN(xb_ld(&bar[XB_TOPGEN]) == tg, bar);
;             __builtin_amdgcn_fence(__ATOMIC_ACQUIRE, "agent");
;             xb_add(&bar[XB_XGEN(b.x)], 1u);
;             asm volatile("s_waitcnt vmcnt(0)" ::: "memory");
;         } else {
;             XB_SPIN(xb_ld(&bar[XB_XGEN(b.x)]) == gen, bar);
;             __builtin_amdgcn_fence(__ATOMIC_ACQUIRE, "agent");
;             asm volatile("s_waitcnt vmcnt(0)" ::: "memory");
;         }
;     }
;     __syncthreads();
; }
.LBB0_186:
	s_load_dwordx2 s[16:17], s[96:97], 0xa0
	s_lshl_b32 s6, s0, 2
	s_add_u32 s6, s10, s6
	s_addc_u32 s7, s11, 0
	s_add_u32 s6, s6, 0x1400
	s_addc_u32 s7, s7, 0
	v_mov_b32_e32 v1, 0
	v_mov_b32_e32 v3, 1
	v_mov_b32_e32 v4, 1
	s_waitcnt lgkmcnt(0)
	v_readfirstlane_b32 s15, v2
	v_readfirstlane_b32 s18, v0
	v_mov_b32_e32 v4, 1
	global_atomic_add v4, v1, v4, s[6:7] sc0
	buffer_inv sc1
	s_add_u32 s12, s16, 0x7400
	s_addc_u32 s13, s17, 0
	s_add_i32 s98, s98, 1
	s_mul_i32 s8, s98, s15
	s_mul_i32 s9, s98, s18
	s_mov_b32 s14, 0
	s_waitcnt vmcnt(1)
	v_readfirstlane_b32 s19, v4
	s_add_i32 s19, s19, 1
	s_cmp_lg_u32 s19, s8
	s_cbranch_scc1 .Lgb0_poll
	buffer_wbl2 sc1
	s_waitcnt vmcnt(0)
	global_atomic_add v1, v3, s[12:13]
.Lgb0_poll:
	global_load_dword v4, v1, s[12:13] sc1
	s_waitcnt vmcnt(0)
	v_readfirstlane_b32 s19, v4
	s_sub_i32 s19, s19, s9
	s_cmp_ge_i32 s19, 0
	s_cbranch_scc1 .Lgb0_done
	s_sleep 1
	s_add_i32 s14, s14, 1
	s_and_b32 s19, s14, 0xff
	s_cmp_lg_u32 s19, 0
	s_cbranch_scc1 .Lgb0_poll
	global_load_dword v4, v1, s[4:5] sc1
	s_waitcnt vmcnt(0)
	v_readfirstlane_b32 s19, v4
	s_cmp_lg_u32 s19, 0
	s_cbranch_scc1 .Lgb0_done
	s_cmp_lt_u32 s14, 0x40001
	s_cbranch_scc1 .Lgb0_poll
	global_atomic_add v1, v3, s[4:5]
.Lgb0_done:
	s_waitcnt vmcnt(0)
.LBB0_222:
	s_or_b64 exec, exec, s[2:3]
	s_waitcnt lgkmcnt(0)
	s_barrier

; __device__ __forceinline__ unsigned xb_ld(unsigned* p)              { return __hip_atomic_load(p, __ATOMIC_RELAXED, __HIP_MEMORY_SCOPE_AGENT); }
; __device__ __forceinline__ unsigned xb_add(unsigned* p, unsigned v) { return __hip_atomic_fetch_add(p, v, __ATOMIC_RELAXED, __HIP_MEMORY_SCOPE_AGENT); }
; #define XB_SPIN(cond, bar) do { unsigned _sp = 0; while (cond) { __builtin_amdgcn_s_sleep(1); \
;     if ((++_sp & 255u) == 0u) { if (xb_ld(&(bar)[XB_TMO])) break; if (_sp > XB_SPIN_CAP) { atomicAdd(&(bar)[XB_TMO], 1u); break; } } } } while (0)
; #define XB_TID() ((int)__builtin_amdgcn_mbcnt_hi(~0u, __builtin_amdgcn_mbcnt_lo(~0u, 0u)) + 64 * xb_wave_id)
; __device__ __forceinline__ void xcd_barrier(const XcdBarrier& b, const int xb_wave_id) {
;     asm volatile("s_waitcnt vmcnt(0)" ::: "memory");
;     __syncthreads();
;     if (XB_TID() == 0) {
;         unsigned* bar = b.bar;
;         __builtin_amdgcn_s_waitcnt(0);
;         unsigned nloc = b.st[0], nx = b.st[1];
;         if (nloc == 0u) { xcd_barrier_complete(bar, b.x, nloc, nx); b.st[0] = nloc; b.st[1] = nx; }
;         const unsigned old = xb_add(&bar[XB_XSUB(b.x)], 1u);
;         const unsigned gen = old / nloc;
;         if (old + 1u == (gen + 1u) * nloc) {
;             __builtin_amdgcn_fence(__ATOMIC_RELEASE, "agent");
;             asm volatile("s_waitcnt vmcnt(0)" ::: "memory");
;             const unsigned og = xb_add(&bar[XB_TOP], 1u);
;             const unsigned tg = og / nx;
;             if (og + 1u == (tg + 1u) * nx) xb_add(&bar[XB_TOPGEN], 1u);
;             else XB_SPIN(xb_ld(&bar[XB_TOPGEN]) == tg, bar);
;             __builtin_amdgcn_fence(__ATOMIC_ACQUIRE, "agent");
;             xb_add(&bar[XB_XGEN(b.x)], 1u);
;             asm volatile("s_waitcnt vmcnt(0)" ::: "memory");
;         } else {
;             XB_SPIN(xb_ld(&bar[XB_XGEN(b.x)]) == gen, bar);
;             __builtin_amdgcn_fence(__ATOMIC_ACQUIRE, "agent");
;             asm volatile("s_waitcnt vmcnt(0)" ::: "memory");
;         }
;     }
;     __syncthreads();
; }
.LBB0_257:
	v_readlane_b32 s2, v251, 41
	v_readlane_b32 s3, v251, 42
	v_mov_b32_e32 v4, 1
	v_mov_b32_e32 v5, 1
	s_waitcnt lgkmcnt(0)
	v_readfirstlane_b32 s4, v3
	v_readfirstlane_b32 s5, v2
	s_nop 1
	v_mov_b32_e32 v4, 1
	global_atomic_add v4, v1, v4, s[2:3] sc0
	buffer_inv sc1
	s_add_i32 s98, s98, 1
	s_mul_i32 s8, s98, s4
	s_mul_i32 s9, s98, s5
	v_readlane_b32 s12, v251, 45
	v_readlane_b32 s13, v251, 46
	s_mov_b32 s14, 0
	s_waitcnt vmcnt(1)
	v_readfirstlane_b32 s15, v4
	s_add_i32 s15, s15, 1
	s_cmp_lg_u32 s15, s8
	s_cbranch_scc1 .Lgb1_poll
	buffer_wbl2 sc1
	s_waitcnt vmcnt(0)
	global_atomic_add v1, v5, s[12:13]
.Lgb1_poll:
	global_load_dword v4, v1, s[12:13] sc1
	s_waitcnt vmcnt(0)
	v_readfirstlane_b32 s15, v4
	s_sub_i32 s15, s15, s9
	s_cmp_ge_i32 s15, 0
	s_cbranch_scc1 .Lgb1_done
	s_sleep 1
	s_add_i32 s14, s14, 1
	s_and_b32 s15, s14, 0xff
	s_cmp_lg_u32 s15, 0
	s_cbranch_scc1 .Lgb1_poll
	global_load_dword v4, v1, s[48:49] sc1
	s_waitcnt vmcnt(0)
	v_readfirstlane_b32 s15, v4
	s_cmp_lg_u32 s15, 0
	s_cbranch_scc1 .Lgb1_done
	s_cmp_lt_u32 s14, 0x40001
	s_cbranch_scc1 .Lgb1_poll
	global_atomic_add v1, v5, s[48:49]
.Lgb1_done:
	s_waitcnt vmcnt(0)
.LBB0_293:
	s_or_b64 exec, exec, s[0:1]
	v_readlane_b32 s8, v249, 26
	s_waitcnt lgkmcnt(0)
	s_barrier
	v_readlane_b32 s9, v249, 27

; __device__ __forceinline__ unsigned xb_ld(unsigned* p)              { return __hip_atomic_load(p, __ATOMIC_RELAXED, __HIP_MEMORY_SCOPE_AGENT); }
; #define XB_SPIN(cond, bar) do { unsigned _sp = 0; while (cond) { __builtin_amdgcn_s_sleep(1); \
;     if ((++_sp & 255u) == 0u) { if (xb_ld(&(bar)[XB_TMO])) break; if (_sp > XB_SPIN_CAP) { atomicAdd(&(bar)[XB_TMO], 1u); break; } } } } while (0)
; __device__ __forceinline__ void xcd_barrier(const XcdBarrier& b, const int xb_wave_id) {
;     ...
;             XB_SPIN(xb_ld(&bar[XB_XGEN(b.x)]) == gen, bar);
;             __builtin_amdgcn_fence(__ATOMIC_ACQUIRE, "agent");
;             asm volatile("s_waitcnt vmcnt(0)" ::: "memory");
;         }
;     }
;     __syncthreads();
.Lgb2_done:
	s_waitcnt vmcnt(0)
.LBB0_562:
	s_or_b64 exec, exec, s[0:1]
	s_waitcnt lgkmcnt(0)
	s_barrier

; __device__ __forceinline__ unsigned xb_ld(unsigned* p)              { return __hip_atomic_load(p, __ATOMIC_RELAXED, __HIP_MEMORY_SCOPE_AGENT); }
; #define XB_SPIN(cond, bar) do { unsigned _sp = 0; while (cond) { __builtin_amdgcn_s_sleep(1); \
;     if ((++_sp & 255u) == 0u) { if (xb_ld(&(bar)[XB_TMO])) break; if (_sp > XB_SPIN_CAP) { atomicAdd(&(bar)[XB_TMO], 1u); break; } } } } while (0)
; __device__ __forceinline__ void xcd_barrier(const XcdBarrier& b, const int xb_wave_id) {
;     ...
;             XB_SPIN(xb_ld(&bar[XB_XGEN(b.x)]) == gen, bar);
;             __builtin_amdgcn_fence(__ATOMIC_ACQUIRE, "agent");
;             asm volatile("s_waitcnt vmcnt(0)" ::: "memory");
;         }
;     }
;     __syncthreads();
.Lgb3_done:
	s_waitcnt vmcnt(0)
.LBB0_851:
	s_or_b64 exec, exec, s[0:1]
	s_waitcnt lgkmcnt(0)
	s_barrier

; __device__ __forceinline__ unsigned xb_ld(unsigned* p)              { return __hip_atomic_load(p, __ATOMIC_RELAXED, __HIP_MEMORY_SCOPE_AGENT); }
; #define XB_SPIN(cond, bar) do { unsigned _sp = 0; while (cond) { __builtin_amdgcn_s_sleep(1); \
;     if ((++_sp & 255u) == 0u) { if (xb_ld(&(bar)[XB_TMO])) break; if (_sp > XB_SPIN_CAP) { atomicAdd(&(bar)[XB_TMO], 1u); break; } } } } while (0)
; __device__ __forceinline__ void xcd_barrier(const XcdBarrier& b, const int xb_wave_id) {
;     ...
;             XB_SPIN(xb_ld(&bar[XB_XGEN(b.x)]) == gen, bar);
;             __builtin_amdgcn_fence(__ATOMIC_ACQUIRE, "agent");
;             asm volatile("s_waitcnt vmcnt(0)" ::: "memory");
;         }
;     }
;     __syncthreads();
.Lgb4_done:
	s_waitcnt vmcnt(0)
.LBB0_914:
	s_or_b64 exec, exec, s[0:1]
	s_waitcnt lgkmcnt(0)
	s_barrier
